# chunk-carry prefix loops: batched loads with counted vmcnt instead of one serialized round trip per step; plus earlier epilogue/tile-balance/XCD-deal edits
# speedup vs baseline: 1.0231x; 1.0231x over previous
; DEVI void ret_decays(int h, float& ldf, float& ldb) { ldf = log1pf(-exp2f(-(5.f + 2.f * h))); ldb = log1pf(-exp2f(-(6.f + 2.f * h))); }
; DEVI void phase_prefix(const Params& p, char* smem, int widx, int nworkers) {
;     ...
;             const int g2 = g - NT_G, seq = g2 >> 12, e4 = (g2 & 4095) * 4;
;             const int h = (seq >> 1) & 3, dir = seq & 1;
;             float ldf, ldb; ret_decays(h, ldf, ldb);
;             const float dd = __expf(64.f * (dir ? ldb : ldf));
.LBB0_602:
	s_mov_b32 s4, 0xffff
	v_lshrrev_b32_e32 v1, 2, v17
	v_cmp_lt_i32_e32 vcc, s4, v16
	s_and_saveexec_b64 s[4:5], vcc
	s_xor_b64 s[56:57], exec, s[4:5]
	s_mov_b32 s14, 0x484c6000
	s_mov_b32 s16, 0x4dec6000
	s_mov_b32 s17, 0x484ce000
	s_mov_b32 s18, 0x4dece000
	s_mov_b32 s23, 0x484d6000
	s_mov_b32 s24, 0x4ded6000
	s_mov_b32 s25, 0x484de000
	s_mov_b32 s28, 0x4dede000
	s_mov_b32 s29, 0x484e6000
	s_mov_b32 s34, 0x4dee6000
	s_mov_b32 s35, 0x484ee000
	s_mov_b32 s44, 0x4deee000
	s_mov_b32 s45, 0x484f6000
	s_mov_b32 s52, 0x4def6000
	s_mov_b32 s58, 0x484fe000
	s_mov_b32 s59, 0x4defe000
	s_mov_b32 s50, 0x4df06000
	s_cbranch_execz .LBB0_605
	v_lshrrev_b32_e32 v2, 12, v16
	v_and_b32_e32 v2, 6, v2
	s_waitcnt vmcnt(0)
	v_add_u32_e32 v4, 5, v2
	v_cvt_f32_ubyte0_e32 v4, v4
	s_mov_b32 s4, 0x42fc0000
	v_cmp_lt_f32_e32 vcc, s4, v4
	s_mov_b32 s5, 0x3f2aaaab
	s_mov_b32 s6, 0x3f317218
	v_cndmask_b32_e32 v5, 0, v226, vcc
	v_sub_f32_e32 v4, v5, v4
	v_exp_f32_e32 v4, v4
	v_cndmask_b32_e32 v5, 0, v235, vcc
	v_add_u32_e32 v2, 6, v2
	v_cvt_f32_ubyte0_e32 v2, v2
	v_ldexp_f32 v21, v4, v5
	v_sub_f32_e32 v6, 1.0, v21
	v_add_f32_e32 v4, -1.0, v6
	v_sub_f32_e32 v5, v4, v6
	v_add_f32_e32 v5, 1.0, v5
	v_sub_f32_e64 v4, -v21, v4
	v_add_f32_e32 v7, v4, v5
	v_frexp_mant_f32_e32 v8, v6
	v_cvt_f64_f32_e32 v[4:5], v6
	v_frexp_exp_i32_f64_e32 v4, v[4:5]
	v_cmp_gt_f32_e32 vcc, s5, v8
	v_add_u32_e32 v20, 0xffff0000, v16
	v_and_b32_e32 v1, 0xfff, v1
	v_subbrev_co_u32_e32 v12, vcc, 0, v4, vcc
	v_sub_u32_e32 v4, 0, v12
	v_ldexp_f32 v5, v6, v4
	v_add_f32_e32 v6, -1.0, v5
	v_add_f32_e32 v8, 1.0, v5
	v_ldexp_f32 v4, v7, v4
	v_add_f32_e32 v7, 1.0, v6
	v_add_f32_e32 v9, -1.0, v8
	v_sub_f32_e32 v7, v5, v7
	v_sub_f32_e32 v5, v5, v9
	v_add_f32_e32 v7, v4, v7
	v_add_f32_e32 v4, v4, v5
	v_add_f32_e32 v13, v8, v4
	v_rcp_f32_e32 v15, v13
	v_sub_f32_e32 v5, v13, v8
	v_sub_f32_e32 v14, v4, v5
	v_add_f32_e32 v5, v6, v7
	v_mul_f32_e32 v19, v5, v15
	v_sub_f32_e32 v4, v5, v6
	v_mul_f32_e32 v6, v13, v19
	v_fma_f32 v8, v19, v13, -v6
	v_fmac_f32_e32 v8, v19, v14
	v_sub_f32_e32 v18, v7, v4
	v_add_f32_e32 v4, v6, v8
	v_sub_f32_e32 v7, v5, v4
	v_pk_add_f32 v[10:11], v[4:5], v[6:7] neg_lo:[0,1] neg_hi:[0,1]
	v_mov_b32_e32 v9, v4
	v_pk_add_f32 v[4:5], v[10:11], v[8:9] neg_lo:[0,1] neg_hi:[0,1]
	v_cmp_nlt_f32_e32 vcc, 1.0, v21
	v_add_f32_e32 v5, v18, v5
	v_add_f32_e32 v4, v4, v5
	v_add_f32_e32 v5, v7, v4
	v_mul_f32_e32 v18, v15, v5
	v_mul_f32_e32 v6, v13, v18
	v_fma_f32 v8, v18, v13, -v6
	v_fmac_f32_e32 v8, v18, v14
	v_sub_f32_e32 v7, v7, v5
	v_add_f32_e32 v13, v4, v7
	v_add_f32_e32 v4, v6, v8
	v_sub_f32_e32 v7, v5, v4
	v_pk_add_f32 v[10:11], v[4:5], v[6:7] neg_lo:[0,1] neg_hi:[0,1]
	v_mov_b32_e32 v9, v4
	v_pk_add_f32 v[4:5], v[10:11], v[8:9] neg_lo:[0,1] neg_hi:[0,1]
	s_nop 0
	v_add_f32_e32 v5, v13, v5
	v_add_f32_e32 v4, v4, v5
	v_add_f32_e32 v5, v19, v18
	v_add_f32_e32 v4, v7, v4
	v_sub_f32_e32 v6, v5, v19
	v_mul_f32_e32 v4, v15, v4
	v_sub_f32_e32 v6, v18, v6
	v_add_f32_e32 v6, v6, v4
	v_add_f32_e32 v8, v5, v6
	v_mul_f32_e32 v9, v8, v8
	v_fmamk_f32 v4, v9, 0x3e9b6dac, v224
	v_fmaak_f32 v197, v9, v4, 0x3f2aaada
	v_cvt_f32_i32_e32 v4, v12
	v_sub_f32_e32 v5, v8, v5
	v_sub_f32_e32 v5, v6, v5
	v_ldexp_f32 v10, v5, 1
	v_mul_f32_e32 v5, v8, v9
	v_ldexp_f32 v7, v8, 1
	v_pk_mul_f32 v[8:9], v[4:5], v[196:197]
	s_nop 0
	v_fma_f32 v6, v4, s6, -v8
	v_fmac_f32_e32 v6, 0xb102e308, v4
	v_pk_add_f32 v[4:5], v[8:9], v[6:7]
	s_nop 0
	v_sub_f32_e32 v7, v5, v7
	v_sub_f32_e32 v7, v9, v7
	v_add_f32_e32 v11, v10, v7
	v_mov_b32_e32 v10, v8
	v_pk_add_f32 v[8:9], v[4:5], v[8:9] neg_lo:[0,1] neg_hi:[0,1]
	v_pk_add_f32 v[12:13], v[4:5], v[10:11]
	v_mov_b32_e32 v7, v4
	v_mov_b32_e32 v9, v13
	v_pk_add_f32 v[14:15], v[6:7], v[8:9] neg_lo:[0,1] neg_hi:[0,1]
	v_pk_add_f32 v[6:7], v[6:7], v[8:9]
	v_mov_b32_e32 v10, v11
	v_pk_add_f32 v[8:9], v[6:7], v[4:5] op_sel:[1,0] op_sel_hi:[0,1] neg_lo:[0,1] neg_hi:[0,1]
	v_pk_add_f32 v[18:19], v[12:13], v[8:9] op_sel_hi:[1,0] neg_lo:[0,1] neg_hi:[0,1]
	v_mov_b32_e32 v12, v13
	v_mov_b32_e32 v13, v7
	v_pk_mov_b32 v[8:9], v[4:5], v[8:9] op_sel:[1,0]
	v_mov_b32_e32 v11, v4
	v_pk_add_f32 v[8:9], v[12:13], v[8:9] neg_lo:[0,1] neg_hi:[0,1]
	v_mov_b32_e32 v18, v14
	v_pk_add_f32 v[4:5], v[10:11], v[8:9] neg_lo:[0,1] neg_hi:[0,1]
	v_mov_b32_e32 v15, v7
	v_pk_add_f32 v[8:9], v[18:19], v[4:5]
	s_nop 0
	v_pk_add_f32 v[10:11], v[8:9], v[8:9] op_sel:[0,1] op_sel_hi:[1,0]
	s_nop 0
	v_pk_add_f32 v[6:7], v[6:7], v[10:11] op_sel:[1,0] op_sel_hi:[0,1]
	v_mov_b32_e32 v9, v6
	v_pk_add_f32 v[12:13], v[8:9], v[14:15] neg_lo:[0,1] neg_hi:[0,1]
	v_mov_b32_e32 v5, v10
	v_sub_f32_e32 v7, v8, v12
	v_pk_add_f32 v[4:5], v[4:5], v[12:13] neg_lo:[0,1] neg_hi:[0,1]
	v_sub_f32_e32 v7, v14, v7
	v_add_f32_e32 v4, v4, v7
	v_add_f32_e32 v4, v4, v5
	v_add_f32_e32 v4, v6, v4
	v_cndmask_b32_e32 v4, v231, v4, vcc
	v_cmp_neq_f32_e32 vcc, 1.0, v21
	s_nop 1
	v_cndmask_b32_e32 v4, v234, v4, vcc
	v_cmp_lt_f32_e32 vcc, s4, v2
	s_mov_b32 s4, 0x33800000
	v_cmp_gt_f32_e64 s[38:39], s4, v21
	v_cndmask_b32_e32 v5, 0, v226, vcc
	v_sub_f32_e32 v2, v5, v2
	v_exp_f32_e32 v2, v2
	v_cndmask_b32_e64 v21, v4, -v21, s[38:39]
	v_cndmask_b32_e32 v4, 0, v235, vcc
	s_mov_b64 s[38:39], 0
	v_ldexp_f32 v2, v2, v4
	v_sub_f32_e32 v6, 1.0, v2
	v_add_f32_e32 v4, -1.0, v6
	v_sub_f32_e32 v5, v4, v6
	v_add_f32_e32 v5, 1.0, v5
	v_sub_f32_e64 v4, -v2, v4
	v_add_f32_e32 v7, v4, v5
	v_frexp_mant_f32_e32 v8, v6
	v_cvt_f64_f32_e32 v[4:5], v6
	v_frexp_exp_i32_f64_e32 v4, v[4:5]
	v_cmp_gt_f32_e32 vcc, s5, v8
	s_mov_b32 s5, 0x4deae000
	s_nop 0
	v_subbrev_co_u32_e32 v12, vcc, 0, v4, vcc
	v_sub_u32_e32 v4, 0, v12
	v_ldexp_f32 v5, v6, v4
	v_add_f32_e32 v6, -1.0, v5
	v_add_f32_e32 v8, 1.0, v5
; DEVI void phase_prefix(const Params& p, char* smem, int widx, int nworkers) {
;     ...
;             const float dd = __expf(64.f * (dir ? ldb : ldf));
;             const bf16_t* U = (const bf16_t*)(p.ws + WS_UTR) + (size_t)seq * NCH * 16384 + e4;
;             bf16_t* S = (bf16_t*)(p.ws + WS_STR) + (size_t)seq * NCH * 16384 + e4;
;             f32x4 st = {0.f, 0.f, 0.f, 0.f};
	v_ldexp_f32 v4, v7, v4
	v_add_f32_e32 v7, 1.0, v6
	v_add_f32_e32 v9, -1.0, v8
	v_sub_f32_e32 v7, v5, v7
	v_sub_f32_e32 v5, v5, v9
	v_add_f32_e32 v7, v4, v7
	v_add_f32_e32 v4, v4, v5
	v_add_f32_e32 v13, v8, v4
	v_rcp_f32_e32 v15, v13
	v_sub_f32_e32 v5, v13, v8
	v_sub_f32_e32 v14, v4, v5
	v_add_f32_e32 v5, v6, v7
	v_mul_f32_e32 v19, v5, v15
	v_sub_f32_e32 v4, v5, v6
	v_mul_f32_e32 v6, v13, v19
	v_fma_f32 v8, v19, v13, -v6
	v_fmac_f32_e32 v8, v19, v14
	v_sub_f32_e32 v18, v7, v4
	v_add_f32_e32 v4, v6, v8
	v_sub_f32_e32 v7, v5, v4
	v_pk_add_f32 v[10:11], v[4:5], v[6:7] neg_lo:[0,1] neg_hi:[0,1]
	v_mov_b32_e32 v9, v4
	v_pk_add_f32 v[4:5], v[10:11], v[8:9] neg_lo:[0,1] neg_hi:[0,1]
	v_cmp_nlt_f32_e32 vcc, 1.0, v2
	v_add_f32_e32 v5, v18, v5
	v_add_f32_e32 v4, v4, v5
	v_add_f32_e32 v5, v7, v4
	v_mul_f32_e32 v18, v15, v5
	v_mul_f32_e32 v6, v13, v18
	v_fma_f32 v8, v18, v13, -v6
	v_fmac_f32_e32 v8, v18, v14
	v_sub_f32_e32 v7, v7, v5
	v_add_f32_e32 v13, v4, v7
	v_add_f32_e32 v4, v6, v8
	v_sub_f32_e32 v7, v5, v4
	v_pk_add_f32 v[10:11], v[4:5], v[6:7] neg_lo:[0,1] neg_hi:[0,1]
	v_mov_b32_e32 v9, v4
	v_pk_add_f32 v[4:5], v[10:11], v[8:9] neg_lo:[0,1] neg_hi:[0,1]
	s_nop 0
	v_add_f32_e32 v5, v13, v5
	v_add_f32_e32 v4, v4, v5
	v_add_f32_e32 v5, v19, v18
	v_add_f32_e32 v4, v7, v4
	v_sub_f32_e32 v6, v5, v19
	v_mul_f32_e32 v4, v15, v4
	v_sub_f32_e32 v6, v18, v6
	v_add_f32_e32 v6, v6, v4
	v_add_f32_e32 v8, v5, v6
	v_mul_f32_e32 v9, v8, v8
	v_fmamk_f32 v4, v9, 0x3e9b6dac, v224
	v_fmaak_f32 v197, v9, v4, 0x3f2aaada
	v_cvt_f32_i32_e32 v4, v12
	v_sub_f32_e32 v5, v8, v5
	v_sub_f32_e32 v5, v6, v5
	v_ldexp_f32 v10, v5, 1
	v_mul_f32_e32 v5, v8, v9
	v_ldexp_f32 v7, v8, 1
	v_pk_mul_f32 v[8:9], v[4:5], v[196:197]
	s_nop 0
	v_fma_f32 v6, v4, s6, -v8
	v_fmac_f32_e32 v6, 0xb102e308, v4
	v_pk_add_f32 v[4:5], v[8:9], v[6:7]
	s_nop 0
	v_sub_f32_e32 v7, v5, v7
	v_sub_f32_e32 v7, v9, v7
	v_add_f32_e32 v11, v10, v7
	v_mov_b32_e32 v10, v8
	v_pk_add_f32 v[8:9], v[4:5], v[8:9] neg_lo:[0,1] neg_hi:[0,1]
	v_pk_add_f32 v[12:13], v[4:5], v[10:11]
	v_mov_b32_e32 v7, v4
	v_mov_b32_e32 v9, v13
	v_pk_add_f32 v[14:15], v[6:7], v[8:9] neg_lo:[0,1] neg_hi:[0,1]
	v_pk_add_f32 v[6:7], v[6:7], v[8:9]
	v_mov_b32_e32 v10, v11
	v_pk_add_f32 v[8:9], v[6:7], v[4:5] op_sel:[1,0] op_sel_hi:[0,1] neg_lo:[0,1] neg_hi:[0,1]
	v_pk_add_f32 v[18:19], v[12:13], v[8:9] op_sel_hi:[1,0] neg_lo:[0,1] neg_hi:[0,1]
	v_mov_b32_e32 v12, v13
	v_mov_b32_e32 v13, v7
	v_pk_mov_b32 v[8:9], v[4:5], v[8:9] op_sel:[1,0]
	v_mov_b32_e32 v11, v4
	v_pk_add_f32 v[8:9], v[12:13], v[8:9] neg_lo:[0,1] neg_hi:[0,1]
	v_mov_b32_e32 v18, v14
	v_pk_add_f32 v[4:5], v[10:11], v[8:9] neg_lo:[0,1] neg_hi:[0,1]
	v_mov_b32_e32 v15, v7
	v_pk_add_f32 v[8:9], v[18:19], v[4:5]
	s_nop 0
	v_pk_add_f32 v[10:11], v[8:9], v[8:9] op_sel:[0,1] op_sel_hi:[1,0]
	s_nop 0
	v_pk_add_f32 v[6:7], v[6:7], v[10:11] op_sel:[1,0] op_sel_hi:[0,1]
	v_mov_b32_e32 v9, v6
	v_pk_add_f32 v[12:13], v[8:9], v[14:15] neg_lo:[0,1] neg_hi:[0,1]
	v_mov_b32_e32 v5, v10
	v_sub_f32_e32 v7, v8, v12
	v_pk_add_f32 v[4:5], v[4:5], v[12:13] neg_lo:[0,1] neg_hi:[0,1]
	v_sub_f32_e32 v7, v14, v7
	v_add_f32_e32 v4, v4, v7
	v_add_f32_e32 v4, v4, v5
	v_add_f32_e32 v4, v6, v4
	v_cndmask_b32_e32 v4, v231, v4, vcc
	v_cmp_neq_f32_e32 vcc, 1.0, v2
	v_mov_b32_e32 v10, 0
	v_mov_b32_e32 v11, v10
	v_cndmask_b32_e32 v4, v234, v4, vcc
	v_cmp_gt_f32_e32 vcc, s4, v2
	v_mov_b32_e32 v12, v10
	v_mov_b32_e32 v13, v10
	v_cndmask_b32_e64 v2, v4, -v2, vcc
	v_and_b32_e32 v4, 0x1000, v16
	v_cmp_eq_u32_e32 vcc, 0, v4
	s_nop 1
	v_cndmask_b32_e32 v2, v2, v21, vcc
	v_mul_f32_e32 v2, 0x42800000, v2
	v_mul_f32_e32 v2, 0x3fb8aa3b, v2
	v_exp_f32_e32 v4, v2
	v_lshrrev_b32_e32 v2, 12, v20
	v_mul_u32_u24_e32 v2, 36, v2
	v_lshlrev_b64 v[8:9], 15, v[2:3]
	v_lshl_or_b32 v8, v1, 3, v8
	v_mov_b32_e32 v5, v4
	v_mov_b32_e32 v6, v4
	v_mov_b32_e32 v7, v4
	v_mov_b32_e32 v100, v8
	v_lshl_add_u64 v[8:9], s[82:83], 0, v[8:9]
; DEVI unsigned cvt_pk(float lo, float hi) { f32x2 v = {lo, hi}; bf16x2_t b = __builtin_convertvector(v, bf16x2_t); return __builtin_bit_cast(unsigned, b); }
; DEVI float bflo(unsigned w) { return __uint_as_float(w << 16); }
; DEVI float bfhi(unsigned w) { return __uint_as_float(w & 0xffff0000u); }
; DEVI void phase_prefix(const Params& p, char* smem, int widx, int nworkers) {
;     ...
; #pragma unroll 12
;             for (int o = 0; o < NCH; ++o) {
;                 const u32x2 uw = *(const u32x2*)(U + (size_t)o * 16384); const f32x4 u = {bflo(uw[0]), bfhi(uw[0]), bflo(uw[1]), bfhi(uw[1])};
;                 *(u32x2*)(S + (size_t)o * 16384) = (u32x2){cvt_pk(st[0], st[1]), cvt_pk(st[2], st[3])};
;                 st = dd * st + u;
;             }
.LBB0_604:
	s_add_u32 s4, s82, 0x484ae000
	s_addc_u32 s5, s83, 0
	s_add_u32 s6, s82, 0x4deae000
	s_addc_u32 s7, s83, 0
	v_add_u32_e32 v101, s38, v100
	global_load_dwordx2 v[52:53], v101, s[4:5]
	v_add_u32_e32 v102, 0x8000, v101
	global_load_dwordx2 v[54:55], v102, s[4:5]
	v_add_u32_e32 v102, 0x10000, v101
	global_load_dwordx2 v[56:57], v102, s[4:5]
	v_add_u32_e32 v102, 0x18000, v101
	global_load_dwordx2 v[58:59], v102, s[4:5]
	v_add_u32_e32 v102, 0x20000, v101
	global_load_dwordx2 v[60:61], v102, s[4:5]
	v_add_u32_e32 v102, 0x28000, v101
	global_load_dwordx2 v[62:63], v102, s[4:5]
	v_add_u32_e32 v102, 0x30000, v101
	global_load_dwordx2 v[64:65], v102, s[4:5]
	v_add_u32_e32 v102, 0x38000, v101
	global_load_dwordx2 v[66:67], v102, s[4:5]
	v_add_u32_e32 v102, 0x40000, v101
	global_load_dwordx2 v[68:69], v102, s[4:5]
	v_add_u32_e32 v102, 0x48000, v101
	global_load_dwordx2 v[70:71], v102, s[4:5]
	v_add_u32_e32 v102, 0x50000, v101
	global_load_dwordx2 v[72:73], v102, s[4:5]
	v_add_u32_e32 v102, 0x58000, v101
	global_load_dwordx2 v[74:75], v102, s[4:5]
	v_cvt_pk_bf16_f32 v22, v10, v11
	v_cvt_pk_bf16_f32 v23, v12, v13
	v_add_u32_e32 v102, 0x0, v101
	global_store_dwordx2 v102, v[22:23], s[6:7]
	s_waitcnt vmcnt(12)
	v_lshlrev_b32_e32 v20, 16, v52
	v_and_b32_e32 v21, 0xffff0000, v52
	v_lshlrev_b32_e32 v18, 16, v53
	v_and_b32_e32 v19, 0xffff0000, v53
	v_pk_fma_f32 v[12:13], v[6:7], v[12:13], v[18:19]
	v_pk_fma_f32 v[10:11], v[4:5], v[10:11], v[20:21]
	v_cvt_pk_bf16_f32 v22, v10, v11
	v_cvt_pk_bf16_f32 v23, v12, v13
	v_add_u32_e32 v102, 0x8000, v101
	global_store_dwordx2 v102, v[22:23], s[6:7]
	s_waitcnt vmcnt(12)
	v_lshlrev_b32_e32 v20, 16, v54
	v_and_b32_e32 v21, 0xffff0000, v54
	v_lshlrev_b32_e32 v18, 16, v55
	v_and_b32_e32 v19, 0xffff0000, v55
	v_pk_fma_f32 v[12:13], v[6:7], v[12:13], v[18:19]
	v_pk_fma_f32 v[10:11], v[4:5], v[10:11], v[20:21]
	v_cvt_pk_bf16_f32 v22, v10, v11
	v_cvt_pk_bf16_f32 v23, v12, v13
	v_add_u32_e32 v102, 0x10000, v101
	global_store_dwordx2 v102, v[22:23], s[6:7]
	s_waitcnt vmcnt(12)
	v_lshlrev_b32_e32 v20, 16, v56
	v_and_b32_e32 v21, 0xffff0000, v56
	v_lshlrev_b32_e32 v18, 16, v57
	v_and_b32_e32 v19, 0xffff0000, v57
	v_pk_fma_f32 v[12:13], v[6:7], v[12:13], v[18:19]
	v_pk_fma_f32 v[10:11], v[4:5], v[10:11], v[20:21]
	v_cvt_pk_bf16_f32 v22, v10, v11
	v_cvt_pk_bf16_f32 v23, v12, v13
	v_add_u32_e32 v102, 0x18000, v101
	global_store_dwordx2 v102, v[22:23], s[6:7]
	s_waitcnt vmcnt(12)
	v_lshlrev_b32_e32 v20, 16, v58
	v_and_b32_e32 v21, 0xffff0000, v58
	v_lshlrev_b32_e32 v18, 16, v59
	v_and_b32_e32 v19, 0xffff0000, v59
	v_pk_fma_f32 v[12:13], v[6:7], v[12:13], v[18:19]
	v_pk_fma_f32 v[10:11], v[4:5], v[10:11], v[20:21]
	v_cvt_pk_bf16_f32 v22, v10, v11
	v_cvt_pk_bf16_f32 v23, v12, v13
	v_add_u32_e32 v102, 0x20000, v101
	global_store_dwordx2 v102, v[22:23], s[6:7]
	s_waitcnt vmcnt(12)
	v_lshlrev_b32_e32 v20, 16, v60
	v_and_b32_e32 v21, 0xffff0000, v60
	v_lshlrev_b32_e32 v18, 16, v61
	v_and_b32_e32 v19, 0xffff0000, v61
	v_pk_fma_f32 v[12:13], v[6:7], v[12:13], v[18:19]
	v_pk_fma_f32 v[10:11], v[4:5], v[10:11], v[20:21]
	v_cvt_pk_bf16_f32 v22, v10, v11
	v_cvt_pk_bf16_f32 v23, v12, v13
	v_add_u32_e32 v102, 0x28000, v101
	global_store_dwordx2 v102, v[22:23], s[6:7]
	s_waitcnt vmcnt(12)
	v_lshlrev_b32_e32 v20, 16, v62
	v_and_b32_e32 v21, 0xffff0000, v62
	v_lshlrev_b32_e32 v18, 16, v63
	v_and_b32_e32 v19, 0xffff0000, v63
	v_pk_fma_f32 v[12:13], v[6:7], v[12:13], v[18:19]
	v_pk_fma_f32 v[10:11], v[4:5], v[10:11], v[20:21]
	v_cvt_pk_bf16_f32 v22, v10, v11
	v_cvt_pk_bf16_f32 v23, v12, v13
	v_add_u32_e32 v102, 0x30000, v101
	global_store_dwordx2 v102, v[22:23], s[6:7]
	s_waitcnt vmcnt(12)
	v_lshlrev_b32_e32 v20, 16, v64
	v_and_b32_e32 v21, 0xffff0000, v64
	v_lshlrev_b32_e32 v18, 16, v65
	v_and_b32_e32 v19, 0xffff0000, v65
	v_pk_fma_f32 v[12:13], v[6:7], v[12:13], v[18:19]
	v_pk_fma_f32 v[10:11], v[4:5], v[10:11], v[20:21]
	v_cvt_pk_bf16_f32 v22, v10, v11
	v_cvt_pk_bf16_f32 v23, v12, v13
	v_add_u32_e32 v102, 0x38000, v101
	global_store_dwordx2 v102, v[22:23], s[6:7]
	s_waitcnt vmcnt(12)
	v_lshlrev_b32_e32 v20, 16, v66
	v_and_b32_e32 v21, 0xffff0000, v66
	v_lshlrev_b32_e32 v18, 16, v67
	v_and_b32_e32 v19, 0xffff0000, v67
	v_pk_fma_f32 v[12:13], v[6:7], v[12:13], v[18:19]
	v_pk_fma_f32 v[10:11], v[4:5], v[10:11], v[20:21]
	v_cvt_pk_bf16_f32 v22, v10, v11
	v_cvt_pk_bf16_f32 v23, v12, v13
	v_add_u32_e32 v102, 0x40000, v101
	global_store_dwordx2 v102, v[22:23], s[6:7]
	s_waitcnt vmcnt(12)
	v_lshlrev_b32_e32 v20, 16, v68
	v_and_b32_e32 v21, 0xffff0000, v68
	v_lshlrev_b32_e32 v18, 16, v69
	v_and_b32_e32 v19, 0xffff0000, v69
	v_pk_fma_f32 v[12:13], v[6:7], v[12:13], v[18:19]
	v_pk_fma_f32 v[10:11], v[4:5], v[10:11], v[20:21]
	v_cvt_pk_bf16_f32 v22, v10, v11
	v_cvt_pk_bf16_f32 v23, v12, v13
	v_add_u32_e32 v102, 0x48000, v101
	global_store_dwordx2 v102, v[22:23], s[6:7]
	s_waitcnt vmcnt(12)
	v_lshlrev_b32_e32 v20, 16, v70
	v_and_b32_e32 v21, 0xffff0000, v70
	v_lshlrev_b32_e32 v18, 16, v71
	v_and_b32_e32 v19, 0xffff0000, v71
	v_pk_fma_f32 v[12:13], v[6:7], v[12:13], v[18:19]
	v_pk_fma_f32 v[10:11], v[4:5], v[10:11], v[20:21]
	v_cvt_pk_bf16_f32 v22, v10, v11
	v_cvt_pk_bf16_f32 v23, v12, v13
	v_add_u32_e32 v102, 0x50000, v101
	global_store_dwordx2 v102, v[22:23], s[6:7]
	s_waitcnt vmcnt(12)
	v_lshlrev_b32_e32 v20, 16, v72
	v_and_b32_e32 v21, 0xffff0000, v72
	v_lshlrev_b32_e32 v18, 16, v73
	v_and_b32_e32 v19, 0xffff0000, v73
	v_pk_fma_f32 v[12:13], v[6:7], v[12:13], v[18:19]
	v_pk_fma_f32 v[10:11], v[4:5], v[10:11], v[20:21]
	v_cvt_pk_bf16_f32 v22, v10, v11
	v_cvt_pk_bf16_f32 v23, v12, v13
	v_add_u32_e32 v102, 0x58000, v101
	global_store_dwordx2 v102, v[22:23], s[6:7]
	s_waitcnt vmcnt(12)
	v_lshlrev_b32_e32 v20, 16, v74
	v_and_b32_e32 v21, 0xffff0000, v74
	v_lshlrev_b32_e32 v18, 16, v75
	v_and_b32_e32 v19, 0xffff0000, v75
	v_pk_fma_f32 v[12:13], v[6:7], v[12:13], v[18:19]
	v_pk_fma_f32 v[10:11], v[4:5], v[10:11], v[20:21]
	s_add_u32 s38, s38, 0x60000
	s_addc_u32 s39, s39, 0
	s_cmp_lg_u32 s38, 0x120000
	s_cbranch_scc1 .LBB0_604

; DEVI unsigned cvt_pk(float lo, float hi) { f32x2 v = {lo, hi}; bf16x2_t b = __builtin_convertvector(v, bf16x2_t); return __builtin_bit_cast(unsigned, b); }
; DEVI float bflo(unsigned w) { return __uint_as_float(w << 16); }
; DEVI float bfhi(unsigned w) { return __uint_as_float(w & 0xffff0000u); }
; DEVI void phase_prefix(const Params& p, char* smem, int widx, int nworkers) {
;     ...
;             const int seq = g >> 11, e4 = (g & 2047) * 4, kk = e4 & 63;
;             const bf16_t* U = (const bf16_t*)(p.ws + WS_UTG) + (size_t)seq * NCH * 8192 + e4;
;             bf16_t* S = (bf16_t*)(p.ws + WS_STG) + (size_t)seq * NCH * 8192 + e4;
;             const float* dec = (const float*)(p.ws + WS_DECG) + (size_t)seq * NCH * 64 + kk;
;             f32x4 st = {0.f, 0.f, 0.f, 0.f};
; #pragma unroll 12
;             for (int o = 0; o < NCH; ++o) {
;                 const u32x2 uw = *(const u32x2*)(U + (size_t)o * 8192); const f32x4 u = {bflo(uw[0]), bfhi(uw[0]), bflo(uw[1]), bfhi(uw[1])}; const f32x4 dd = *(const f32x4*)(dec + o * 64);
;                 *(u32x2*)(S + (size_t)o * 8192) = (u32x2){cvt_pk(st[0], st[1]), cvt_pk(st[2], st[3])};
;                 st = dd * st + u;
;             }
.LBB0_607:
	s_add_u32 s4, s82, 0x460ae000
	s_addc_u32 s5, s83, 0
	s_add_u32 s16, s82, 0x4ccae000
	s_addc_u32 s17, s83, 0
	s_add_u32 s24, s82, 0x502ae000
	s_addc_u32 s25, s83, 0
	global_load_dwordx2 v[52:53], v6, s[4:5]
	v_add_u32_e32 v102, 0x4000, v6
	global_load_dwordx2 v[54:55], v102, s[4:5]
	v_add_u32_e32 v102, 0x8000, v6
	global_load_dwordx2 v[56:57], v102, s[4:5]
	v_add_u32_e32 v102, 0xc000, v6
	global_load_dwordx2 v[58:59], v102, s[4:5]
	v_add_u32_e32 v102, 0x10000, v6
	global_load_dwordx2 v[60:61], v102, s[4:5]
	v_add_u32_e32 v102, 0x14000, v6
	global_load_dwordx2 v[62:63], v102, s[4:5]
	v_add_u32_e32 v102, 0x18000, v6
	global_load_dwordx2 v[64:65], v102, s[4:5]
	v_add_u32_e32 v102, 0x1c000, v6
	global_load_dwordx2 v[66:67], v102, s[4:5]
	v_add_u32_e32 v102, 0x20000, v6
	global_load_dwordx2 v[68:69], v102, s[4:5]
	v_add_u32_e32 v102, 0x24000, v6
	global_load_dwordx2 v[70:71], v102, s[4:5]
	v_add_u32_e32 v102, 0x28000, v6
	global_load_dwordx2 v[72:73], v102, s[4:5]
	v_add_u32_e32 v102, 0x2c000, v6
	global_load_dwordx2 v[74:75], v102, s[4:5]
	global_load_dwordx4 v[156:159], v4, s[24:25]
	global_load_dwordx4 v[160:163], v4, s[24:25] offset:256
	global_load_dwordx4 v[164:167], v4, s[24:25] offset:512
	global_load_dwordx4 v[168:171], v4, s[24:25] offset:768
	global_load_dwordx4 v[172:175], v4, s[24:25] offset:1024
	global_load_dwordx4 v[176:179], v4, s[24:25] offset:1280
	global_load_dwordx4 v[198:201], v4, s[24:25] offset:1536
	global_load_dwordx4 v[202:205], v4, s[24:25] offset:1792
	global_load_dwordx4 v[206:209], v4, s[24:25] offset:2048
	global_load_dwordx4 v[210:213], v4, s[24:25] offset:2304
	global_load_dwordx4 v[214:217], v4, s[24:25] offset:2560
	global_load_dwordx4 v[218:221], v4, s[24:25] offset:2816
	v_cvt_pk_bf16_f32 v26, v12, v13
	v_cvt_pk_bf16_f32 v27, v14, v15
	v_add_u32_e32 v102, 0x0, v6
	global_store_dwordx2 v102, v[26:27], s[16:17]
	s_waitcnt vmcnt(12)
	v_lshlrev_b32_e32 v22, 16, v52
	v_and_b32_e32 v23, 0xffff0000, v52
	v_lshlrev_b32_e32 v24, 16, v53
	v_and_b32_e32 v25, 0xffff0000, v53
	v_pk_fma_f32 v[12:13], v[12:13], v[156:157], v[22:23]
	v_pk_fma_f32 v[14:15], v[14:15], v[158:159], v[24:25]
	v_cvt_pk_bf16_f32 v26, v12, v13
	v_cvt_pk_bf16_f32 v27, v14, v15
	v_add_u32_e32 v102, 0x4000, v6
	global_store_dwordx2 v102, v[26:27], s[16:17]
	s_waitcnt vmcnt(12)
	v_lshlrev_b32_e32 v22, 16, v54
	v_and_b32_e32 v23, 0xffff0000, v54
	v_lshlrev_b32_e32 v24, 16, v55
	v_and_b32_e32 v25, 0xffff0000, v55
	v_pk_fma_f32 v[12:13], v[12:13], v[160:161], v[22:23]
	v_pk_fma_f32 v[14:15], v[14:15], v[162:163], v[24:25]
	v_cvt_pk_bf16_f32 v26, v12, v13
	v_cvt_pk_bf16_f32 v27, v14, v15
	v_add_u32_e32 v102, 0x8000, v6
	global_store_dwordx2 v102, v[26:27], s[16:17]
	s_waitcnt vmcnt(12)
	v_lshlrev_b32_e32 v22, 16, v56
	v_and_b32_e32 v23, 0xffff0000, v56
	v_lshlrev_b32_e32 v24, 16, v57
	v_and_b32_e32 v25, 0xffff0000, v57
	v_pk_fma_f32 v[12:13], v[12:13], v[164:165], v[22:23]
	v_pk_fma_f32 v[14:15], v[14:15], v[166:167], v[24:25]
	v_cvt_pk_bf16_f32 v26, v12, v13
	v_cvt_pk_bf16_f32 v27, v14, v15
	v_add_u32_e32 v102, 0xc000, v6
	global_store_dwordx2 v102, v[26:27], s[16:17]
	s_waitcnt vmcnt(12)
	v_lshlrev_b32_e32 v22, 16, v58
	v_and_b32_e32 v23, 0xffff0000, v58
	v_lshlrev_b32_e32 v24, 16, v59
	v_and_b32_e32 v25, 0xffff0000, v59
	v_pk_fma_f32 v[12:13], v[12:13], v[168:169], v[22:23]
	v_pk_fma_f32 v[14:15], v[14:15], v[170:171], v[24:25]
	v_cvt_pk_bf16_f32 v26, v12, v13
	v_cvt_pk_bf16_f32 v27, v14, v15
	v_add_u32_e32 v102, 0x10000, v6
	global_store_dwordx2 v102, v[26:27], s[16:17]
	s_waitcnt vmcnt(12)
	v_lshlrev_b32_e32 v22, 16, v60
	v_and_b32_e32 v23, 0xffff0000, v60
	v_lshlrev_b32_e32 v24, 16, v61
	v_and_b32_e32 v25, 0xffff0000, v61
	v_pk_fma_f32 v[12:13], v[12:13], v[172:173], v[22:23]
	v_pk_fma_f32 v[14:15], v[14:15], v[174:175], v[24:25]
	v_cvt_pk_bf16_f32 v26, v12, v13
	v_cvt_pk_bf16_f32 v27, v14, v15
	v_add_u32_e32 v102, 0x14000, v6
	global_store_dwordx2 v102, v[26:27], s[16:17]
	s_waitcnt vmcnt(12)
	v_lshlrev_b32_e32 v22, 16, v62
	v_and_b32_e32 v23, 0xffff0000, v62
	v_lshlrev_b32_e32 v24, 16, v63
	v_and_b32_e32 v25, 0xffff0000, v63
	v_pk_fma_f32 v[12:13], v[12:13], v[176:177], v[22:23]
	v_pk_fma_f32 v[14:15], v[14:15], v[178:179], v[24:25]
	v_cvt_pk_bf16_f32 v26, v12, v13
	v_cvt_pk_bf16_f32 v27, v14, v15
	v_add_u32_e32 v102, 0x18000, v6
	global_store_dwordx2 v102, v[26:27], s[16:17]
	s_waitcnt vmcnt(12)
	v_lshlrev_b32_e32 v22, 16, v64
	v_and_b32_e32 v23, 0xffff0000, v64
	v_lshlrev_b32_e32 v24, 16, v65
	v_and_b32_e32 v25, 0xffff0000, v65
	v_pk_fma_f32 v[12:13], v[12:13], v[198:199], v[22:23]
	v_pk_fma_f32 v[14:15], v[14:15], v[200:201], v[24:25]
	v_cvt_pk_bf16_f32 v26, v12, v13
	v_cvt_pk_bf16_f32 v27, v14, v15
	v_add_u32_e32 v102, 0x1c000, v6
	global_store_dwordx2 v102, v[26:27], s[16:17]
	s_waitcnt vmcnt(12)
	v_lshlrev_b32_e32 v22, 16, v66
	v_and_b32_e32 v23, 0xffff0000, v66
	v_lshlrev_b32_e32 v24, 16, v67
	v_and_b32_e32 v25, 0xffff0000, v67
	v_pk_fma_f32 v[12:13], v[12:13], v[202:203], v[22:23]
	v_pk_fma_f32 v[14:15], v[14:15], v[204:205], v[24:25]
	v_cvt_pk_bf16_f32 v26, v12, v13
	v_cvt_pk_bf16_f32 v27, v14, v15
	v_add_u32_e32 v102, 0x20000, v6
	global_store_dwordx2 v102, v[26:27], s[16:17]
	s_waitcnt vmcnt(12)
	v_lshlrev_b32_e32 v22, 16, v68
	v_and_b32_e32 v23, 0xffff0000, v68
	v_lshlrev_b32_e32 v24, 16, v69
	v_and_b32_e32 v25, 0xffff0000, v69
	v_pk_fma_f32 v[12:13], v[12:13], v[206:207], v[22:23]
	v_pk_fma_f32 v[14:15], v[14:15], v[208:209], v[24:25]
	v_cvt_pk_bf16_f32 v26, v12, v13
	v_cvt_pk_bf16_f32 v27, v14, v15
	v_add_u32_e32 v102, 0x24000, v6
	global_store_dwordx2 v102, v[26:27], s[16:17]
	s_waitcnt vmcnt(12)
	v_lshlrev_b32_e32 v22, 16, v70
	v_and_b32_e32 v23, 0xffff0000, v70
	v_lshlrev_b32_e32 v24, 16, v71
	v_and_b32_e32 v25, 0xffff0000, v71
	v_pk_fma_f32 v[12:13], v[12:13], v[210:211], v[22:23]
	v_pk_fma_f32 v[14:15], v[14:15], v[212:213], v[24:25]
	v_cvt_pk_bf16_f32 v26, v12, v13
	v_cvt_pk_bf16_f32 v27, v14, v15
	v_add_u32_e32 v102, 0x28000, v6
	global_store_dwordx2 v102, v[26:27], s[16:17]
	s_waitcnt vmcnt(12)
	v_lshlrev_b32_e32 v22, 16, v72
	v_and_b32_e32 v23, 0xffff0000, v72
	v_lshlrev_b32_e32 v24, 16, v73
	v_and_b32_e32 v25, 0xffff0000, v73
	v_pk_fma_f32 v[12:13], v[12:13], v[214:215], v[22:23]
	v_pk_fma_f32 v[14:15], v[14:15], v[216:217], v[24:25]
	v_cvt_pk_bf16_f32 v26, v12, v13
	v_cvt_pk_bf16_f32 v27, v14, v15
	v_add_u32_e32 v102, 0x2c000, v6
	global_store_dwordx2 v102, v[26:27], s[16:17]
	s_waitcnt vmcnt(12)
	v_lshlrev_b32_e32 v22, 16, v74
	v_and_b32_e32 v23, 0xffff0000, v74
	v_lshlrev_b32_e32 v24, 16, v75
	v_and_b32_e32 v25, 0xffff0000, v75
	v_pk_fma_f32 v[12:13], v[12:13], v[218:219], v[22:23]
	v_pk_fma_f32 v[14:15], v[14:15], v[220:221], v[24:25]
	v_add_u32_e32 v6, 0x30000, v6
	v_add_u32_e32 v4, 0xc00, v4
	s_mov_b32 s4, 0x4ccb2000
	s_mov_b32 s5, 0x460b6000
	s_mov_b32 s16, 0x4ccba000
	s_mov_b32 s17, 0x460be000
	s_mov_b32 s24, 0x4ccc2000
	s_mov_b32 s25, 0x460c6000
	s_add_i32 s6, s6, -12
	s_cmp_eq_u32 s6, 0
	s_cbranch_scc0 .LBB0_607
	s_branch .LBB0_601
